# code placement: the eight GEMM K-loop heads pinned to 64-byte boundaries (pad nops executed once per tile); on top of e1
# speedup vs baseline: 1.0003x; 1.0003x over previous
.LBB0_400:
	s_ashr_i32 s15, s14, 31
	s_lshl_b64 s[16:17], s[14:15], 20
	s_add_u32 s16, s38, s16
	s_addc_u32 s17, s39, s17
	s_and_b64 s[18:19], s[8:9], exec
	s_cselect_b32 s15, s17, s21
	s_cselect_b32 s72, s16, s20
	s_ashr_i32 s13, s12, 31
	s_lshl_b64 s[18:19], s[12:13], 20
	s_add_u32 s18, s36, s18
	s_addc_u32 s19, s37, s19
	s_and_b64 s[34:35], s[8:9], exec
	s_cselect_b32 s13, s19, s31
	s_cselect_b32 s73, s18, s30
	s_add_u32 s20, s20, 0x80080
	s_addc_u32 s21, s21, 0
	s_add_u32 s76, s30, 0x100
	v_mov_b32_e32 v0, 0
	s_addc_u32 s77, s31, 0
	s_mov_b32 s84, -2
	v_mov_b32_e32 v1, v0
	v_mov_b32_e32 v2, v0
	v_mov_b32_e32 v3, v0
	v_mov_b32_e32 v4, v0
	v_mov_b32_e32 v5, v0
	v_mov_b32_e32 v6, v0
	v_mov_b32_e32 v7, v0
	v_mov_b32_e32 v8, v0
	v_mov_b32_e32 v9, v0
	v_mov_b32_e32 v10, v0
	v_mov_b32_e32 v11, v0
	v_mov_b32_e32 v16, v0
	v_mov_b32_e32 v17, v0
	v_mov_b32_e32 v18, v0
	v_mov_b32_e32 v19, v0
	v_mov_b32_e32 v24, v0
	v_mov_b32_e32 v25, v0
	v_mov_b32_e32 v26, v0
	v_mov_b32_e32 v27, v0
	v_mov_b32_e32 v32, v0
	v_mov_b32_e32 v33, v0
	v_mov_b32_e32 v34, v0
	v_mov_b32_e32 v35, v0
	v_mov_b32_e32 v40, v0
	v_mov_b32_e32 v41, v0
	v_mov_b32_e32 v42, v0
	v_mov_b32_e32 v43, v0
	v_mov_b32_e32 v48, v0
	v_mov_b32_e32 v49, v0
	v_mov_b32_e32 v50, v0
	v_mov_b32_e32 v51, v0
	v_mov_b32_e32 v12, v0
	v_mov_b32_e32 v13, v0
	v_mov_b32_e32 v14, v0
	v_mov_b32_e32 v15, v0
	v_mov_b32_e32 v20, v0
	v_mov_b32_e32 v21, v0
	v_mov_b32_e32 v22, v0
	v_mov_b32_e32 v23, v0
	v_mov_b32_e32 v28, v0
	v_mov_b32_e32 v29, v0
	v_mov_b32_e32 v30, v0
	v_mov_b32_e32 v31, v0
	v_mov_b32_e32 v36, v0
	v_mov_b32_e32 v37, v0
	v_mov_b32_e32 v38, v0
	v_mov_b32_e32 v39, v0
	v_mov_b32_e32 v44, v0
	v_mov_b32_e32 v45, v0
	v_mov_b32_e32 v46, v0
	v_mov_b32_e32 v47, v0
	v_mov_b32_e32 v52, v0
	v_mov_b32_e32 v53, v0
	v_mov_b32_e32 v54, v0
	v_mov_b32_e32 v55, v0
	v_mov_b32_e32 v56, v0
	v_mov_b32_e32 v57, v0
	v_mov_b32_e32 v58, v0
	v_mov_b32_e32 v59, v0
	v_mov_b32_e32 v60, v0
	v_mov_b32_e32 v61, v0
	v_mov_b32_e32 v62, v0
	v_mov_b32_e32 v63, v0
	v_mov_b32_e32 v64, v0
	v_mov_b32_e32 v65, v0
	v_mov_b32_e32 v66, v0
	v_mov_b32_e32 v67, v0
	v_mov_b32_e32 v68, v0
	v_mov_b32_e32 v69, v0
	v_mov_b32_e32 v70, v0
	v_mov_b32_e32 v71, v0
	v_mov_b32_e32 v72, v0
	v_mov_b32_e32 v73, v0
	v_mov_b32_e32 v74, v0
	v_mov_b32_e32 v75, v0
	v_mov_b32_e32 v80, v0
	v_mov_b32_e32 v81, v0
	v_mov_b32_e32 v82, v0
	v_mov_b32_e32 v83, v0
	v_mov_b32_e32 v88, v0
	v_mov_b32_e32 v89, v0
	v_mov_b32_e32 v90, v0
	v_mov_b32_e32 v91, v0
	v_mov_b32_e32 v92, v0
	v_mov_b32_e32 v93, v0
	v_mov_b32_e32 v94, v0
	v_mov_b32_e32 v95, v0
	v_mov_b32_e32 v104, v0
	v_mov_b32_e32 v105, v0
	v_mov_b32_e32 v106, v0
	v_mov_b32_e32 v107, v0
	v_mov_b32_e32 v108, v0
	v_mov_b32_e32 v109, v0
	v_mov_b32_e32 v110, v0
	v_mov_b32_e32 v111, v0
	v_mov_b32_e32 v76, v0
	v_mov_b32_e32 v77, v0
	v_mov_b32_e32 v78, v0
	v_mov_b32_e32 v79, v0
	v_mov_b32_e32 v84, v0
	v_mov_b32_e32 v85, v0
	v_mov_b32_e32 v86, v0
	v_mov_b32_e32 v87, v0
	v_mov_b32_e32 v96, v0
	v_mov_b32_e32 v97, v0
	v_mov_b32_e32 v98, v0
	v_mov_b32_e32 v99, v0
	v_mov_b32_e32 v100, v0
	v_mov_b32_e32 v101, v0
	v_mov_b32_e32 v102, v0
	v_mov_b32_e32 v103, v0
	v_mov_b32_e32 v112, v0
	v_mov_b32_e32 v113, v0
	v_mov_b32_e32 v114, v0
	v_mov_b32_e32 v115, v0
	v_mov_b32_e32 v116, v0
	v_mov_b32_e32 v117, v0
	v_mov_b32_e32 v118, v0
	v_mov_b32_e32 v119, v0
	v_mov_b32_e32 v120, v0
	v_mov_b32_e32 v121, v0
	v_mov_b32_e32 v122, v0
	v_mov_b32_e32 v123, v0
	v_mov_b32_e32 v124, v0
	v_mov_b32_e32 v125, v0
	v_mov_b32_e32 v126, v0
	v_mov_b32_e32 v127, v0
	.p2alignl 6, 3212836864

.LBB0_500:
	s_ashr_i32 s17, s16, 31
	s_lshl_b64 s[18:19], s[16:17], 20
	s_add_u32 s18, s52, s18
	s_addc_u32 s19, s53, s19
	s_and_b64 s[20:21], s[8:9], exec
	s_cselect_b32 s17, s19, s31
	s_cselect_b32 s76, s18, s30
	s_ashr_i32 s15, s14, 31
	s_lshl_b64 s[20:21], s[14:15], 20
	s_add_u32 s20, s41, s20
	s_addc_u32 s21, s43, s21
	s_and_b64 s[36:37], s[8:9], exec
	s_cselect_b32 s15, s21, s35
	s_cselect_b32 s77, s20, s34
	s_add_u32 s30, s30, 0x80080
	s_addc_u32 s31, s31, 0
	s_add_u32 s84, s34, 0x100
	v_mov_b32_e32 v0, 0
	s_addc_u32 s88, s35, 0
	s_mov_b32 s89, -2
	v_mov_b32_e32 v1, v0
	v_mov_b32_e32 v2, v0
	v_mov_b32_e32 v3, v0
	v_mov_b32_e32 v4, v0
	v_mov_b32_e32 v5, v0
	v_mov_b32_e32 v6, v0
	v_mov_b32_e32 v7, v0
	v_mov_b32_e32 v8, v0
	v_mov_b32_e32 v9, v0
	v_mov_b32_e32 v10, v0
	v_mov_b32_e32 v11, v0
	v_mov_b32_e32 v16, v0
	v_mov_b32_e32 v17, v0
	v_mov_b32_e32 v18, v0
	v_mov_b32_e32 v19, v0
	v_mov_b32_e32 v24, v0
	v_mov_b32_e32 v25, v0
	v_mov_b32_e32 v26, v0
	v_mov_b32_e32 v27, v0
	v_mov_b32_e32 v32, v0
	v_mov_b32_e32 v33, v0
	v_mov_b32_e32 v34, v0
	v_mov_b32_e32 v35, v0
	v_mov_b32_e32 v40, v0
	v_mov_b32_e32 v41, v0
	v_mov_b32_e32 v42, v0
	v_mov_b32_e32 v43, v0
	v_mov_b32_e32 v48, v0
	v_mov_b32_e32 v49, v0
	v_mov_b32_e32 v50, v0
	v_mov_b32_e32 v51, v0
	v_mov_b32_e32 v12, v0
	v_mov_b32_e32 v13, v0
	v_mov_b32_e32 v14, v0
	v_mov_b32_e32 v15, v0
	v_mov_b32_e32 v20, v0
	v_mov_b32_e32 v21, v0
	v_mov_b32_e32 v22, v0
	v_mov_b32_e32 v23, v0
	v_mov_b32_e32 v28, v0
	v_mov_b32_e32 v29, v0
	v_mov_b32_e32 v30, v0
	v_mov_b32_e32 v31, v0
	v_mov_b32_e32 v36, v0
	v_mov_b32_e32 v37, v0
	v_mov_b32_e32 v38, v0
	v_mov_b32_e32 v39, v0
	v_mov_b32_e32 v44, v0
	v_mov_b32_e32 v45, v0
	v_mov_b32_e32 v46, v0
	v_mov_b32_e32 v47, v0
	v_mov_b32_e32 v52, v0
	v_mov_b32_e32 v53, v0
	v_mov_b32_e32 v54, v0
	v_mov_b32_e32 v55, v0
	v_mov_b32_e32 v56, v0
	v_mov_b32_e32 v57, v0
	v_mov_b32_e32 v58, v0
	v_mov_b32_e32 v59, v0
	v_mov_b32_e32 v60, v0
	v_mov_b32_e32 v61, v0
	v_mov_b32_e32 v62, v0
	v_mov_b32_e32 v63, v0
	v_mov_b32_e32 v64, v0
	v_mov_b32_e32 v65, v0
	v_mov_b32_e32 v66, v0
	v_mov_b32_e32 v67, v0
	v_mov_b32_e32 v68, v0
	v_mov_b32_e32 v69, v0
	v_mov_b32_e32 v70, v0
	v_mov_b32_e32 v71, v0
	v_mov_b32_e32 v72, v0
	v_mov_b32_e32 v73, v0
	v_mov_b32_e32 v74, v0
	v_mov_b32_e32 v75, v0
	v_mov_b32_e32 v80, v0
	v_mov_b32_e32 v81, v0
	v_mov_b32_e32 v82, v0
	v_mov_b32_e32 v83, v0
	v_mov_b32_e32 v88, v0
	v_mov_b32_e32 v89, v0
	v_mov_b32_e32 v90, v0
	v_mov_b32_e32 v91, v0
	v_mov_b32_e32 v92, v0
	v_mov_b32_e32 v93, v0
	v_mov_b32_e32 v94, v0
	v_mov_b32_e32 v95, v0
	v_mov_b32_e32 v104, v0
	v_mov_b32_e32 v105, v0
	v_mov_b32_e32 v106, v0
	v_mov_b32_e32 v107, v0
	v_mov_b32_e32 v108, v0
	v_mov_b32_e32 v109, v0
	v_mov_b32_e32 v110, v0
	v_mov_b32_e32 v111, v0
	v_mov_b32_e32 v76, v0
	v_mov_b32_e32 v77, v0
	v_mov_b32_e32 v78, v0
	v_mov_b32_e32 v79, v0
	v_mov_b32_e32 v84, v0
	v_mov_b32_e32 v85, v0
	v_mov_b32_e32 v86, v0
	v_mov_b32_e32 v87, v0
	v_mov_b32_e32 v96, v0
	v_mov_b32_e32 v97, v0
	v_mov_b32_e32 v98, v0
	v_mov_b32_e32 v99, v0
	v_mov_b32_e32 v100, v0
	v_mov_b32_e32 v101, v0
	v_mov_b32_e32 v102, v0
	v_mov_b32_e32 v103, v0
	v_mov_b32_e32 v112, v0
	v_mov_b32_e32 v113, v0
	v_mov_b32_e32 v114, v0
	v_mov_b32_e32 v115, v0
	v_mov_b32_e32 v116, v0
	v_mov_b32_e32 v117, v0
	v_mov_b32_e32 v118, v0
	v_mov_b32_e32 v119, v0
	v_mov_b32_e32 v120, v0
	v_mov_b32_e32 v121, v0
	v_mov_b32_e32 v122, v0
	v_mov_b32_e32 v123, v0
	v_mov_b32_e32 v124, v0
	v_mov_b32_e32 v125, v0
	v_mov_b32_e32 v126, v0
	v_mov_b32_e32 v127, v0
	.p2alignl 6, 3212836864

.LBB0_556:
	s_ashr_i32 s13, s12, 31
	s_lshl_b64 s[14:15], s[12:13], 20
	s_add_u32 s14, s38, s14
	s_addc_u32 s15, s39, s15
	s_and_b64 s[16:17], s[6:7], exec
	s_cselect_b32 s13, s15, s19
	s_cselect_b32 s70, s14, s18
	s_ashr_i32 s11, s10, 31
	s_lshl_b64 s[16:17], s[10:11], 20
	s_add_u32 s16, s34, s16
	s_addc_u32 s17, s35, s17
	s_and_b64 s[30:31], s[6:7], exec
	s_cselect_b32 s11, s17, s21
	s_cselect_b32 s71, s16, s20
	s_add_u32 s18, s18, 0x80080
	s_addc_u32 s19, s19, 0
	s_add_u32 s72, s20, 0x100
	v_mov_b32_e32 v0, 0
	s_addc_u32 s73, s21, 0
	s_mov_b32 s76, -2
	v_mov_b32_e32 v1, v0
	v_mov_b32_e32 v2, v0
	v_mov_b32_e32 v3, v0
	v_mov_b32_e32 v4, v0
	v_mov_b32_e32 v5, v0
	v_mov_b32_e32 v6, v0
	v_mov_b32_e32 v7, v0
	v_mov_b32_e32 v8, v0
	v_mov_b32_e32 v9, v0
	v_mov_b32_e32 v10, v0
	v_mov_b32_e32 v11, v0
	v_mov_b32_e32 v12, v0
	v_mov_b32_e32 v13, v0
	v_mov_b32_e32 v14, v0
	v_mov_b32_e32 v15, v0
	v_mov_b32_e32 v24, v0
	v_mov_b32_e32 v25, v0
	v_mov_b32_e32 v26, v0
	v_mov_b32_e32 v27, v0
	v_mov_b32_e32 v28, v0
	v_mov_b32_e32 v29, v0
	v_mov_b32_e32 v30, v0
	v_mov_b32_e32 v31, v0
	v_mov_b32_e32 v40, v0
	v_mov_b32_e32 v41, v0
	v_mov_b32_e32 v42, v0
	v_mov_b32_e32 v43, v0
	v_mov_b32_e32 v44, v0
	v_mov_b32_e32 v45, v0
	v_mov_b32_e32 v46, v0
	v_mov_b32_e32 v47, v0
	v_mov_b32_e32 v16, v0
	v_mov_b32_e32 v17, v0
	v_mov_b32_e32 v18, v0
	v_mov_b32_e32 v19, v0
	v_mov_b32_e32 v20, v0
	v_mov_b32_e32 v21, v0
	v_mov_b32_e32 v22, v0
	v_mov_b32_e32 v23, v0
	v_mov_b32_e32 v32, v0
	v_mov_b32_e32 v33, v0
	v_mov_b32_e32 v34, v0
	v_mov_b32_e32 v35, v0
	v_mov_b32_e32 v36, v0
	v_mov_b32_e32 v37, v0
	v_mov_b32_e32 v38, v0
	v_mov_b32_e32 v39, v0
	v_mov_b32_e32 v48, v0
	v_mov_b32_e32 v49, v0
	v_mov_b32_e32 v50, v0
	v_mov_b32_e32 v51, v0
	v_mov_b32_e32 v52, v0
	v_mov_b32_e32 v53, v0
	v_mov_b32_e32 v54, v0
	v_mov_b32_e32 v55, v0
	v_mov_b32_e32 v56, v0
	v_mov_b32_e32 v57, v0
	v_mov_b32_e32 v58, v0
	v_mov_b32_e32 v59, v0
	v_mov_b32_e32 v60, v0
	v_mov_b32_e32 v61, v0
	v_mov_b32_e32 v62, v0
	v_mov_b32_e32 v63, v0
	v_mov_b32_e32 v64, v0
	v_mov_b32_e32 v65, v0
	v_mov_b32_e32 v66, v0
	v_mov_b32_e32 v67, v0
	v_mov_b32_e32 v68, v0
	v_mov_b32_e32 v69, v0
	v_mov_b32_e32 v70, v0
	v_mov_b32_e32 v71, v0
	v_mov_b32_e32 v72, v0
	v_mov_b32_e32 v73, v0
	v_mov_b32_e32 v74, v0
	v_mov_b32_e32 v75, v0
	v_mov_b32_e32 v76, v0
	v_mov_b32_e32 v77, v0
	v_mov_b32_e32 v78, v0
	v_mov_b32_e32 v79, v0
	v_mov_b32_e32 v88, v0
	v_mov_b32_e32 v89, v0
	v_mov_b32_e32 v90, v0
	v_mov_b32_e32 v91, v0
	v_mov_b32_e32 v92, v0
	v_mov_b32_e32 v93, v0
	v_mov_b32_e32 v94, v0
	v_mov_b32_e32 v95, v0
	v_mov_b32_e32 v104, v0
	v_mov_b32_e32 v105, v0
	v_mov_b32_e32 v106, v0
	v_mov_b32_e32 v107, v0
	v_mov_b32_e32 v108, v0
	v_mov_b32_e32 v109, v0
	v_mov_b32_e32 v110, v0
	v_mov_b32_e32 v111, v0
	v_mov_b32_e32 v80, v0
	v_mov_b32_e32 v81, v0
	v_mov_b32_e32 v82, v0
	v_mov_b32_e32 v83, v0
	v_mov_b32_e32 v84, v0
	v_mov_b32_e32 v85, v0
	v_mov_b32_e32 v86, v0
	v_mov_b32_e32 v87, v0
	v_mov_b32_e32 v96, v0
	v_mov_b32_e32 v97, v0
	v_mov_b32_e32 v98, v0
	v_mov_b32_e32 v99, v0
	v_mov_b32_e32 v100, v0
	v_mov_b32_e32 v101, v0
	v_mov_b32_e32 v102, v0
	v_mov_b32_e32 v103, v0
	v_mov_b32_e32 v112, v0
	v_mov_b32_e32 v113, v0
	v_mov_b32_e32 v114, v0
	v_mov_b32_e32 v115, v0
	v_mov_b32_e32 v116, v0
	v_mov_b32_e32 v117, v0
	v_mov_b32_e32 v118, v0
	v_mov_b32_e32 v119, v0
	v_mov_b32_e32 v120, v0
	v_mov_b32_e32 v121, v0
	v_mov_b32_e32 v122, v0
	v_mov_b32_e32 v123, v0
	v_mov_b32_e32 v124, v0
	v_mov_b32_e32 v125, v0
	v_mov_b32_e32 v126, v0
	v_mov_b32_e32 v127, v0
	.p2alignl 6, 3212836864

.LBB0_651:
	s_ashr_i32 s13, s12, 31
	s_lshl_b64 s[14:15], s[12:13], 18
	v_readlane_b32 s11, v254, 9
	s_add_u32 s14, s11, s14
	v_readlane_b32 s11, v254, 10
	s_addc_u32 s15, s11, s15
	s_and_b64 s[16:17], s[6:7], exec
	s_cselect_b32 s13, s15, s19
	s_cselect_b32 s36, s14, s18
	s_ashr_i32 s11, s10, 31
	s_lshl_b64 s[16:17], s[10:11], 18
	s_add_u32 s16, s41, s16
	s_addc_u32 s17, s43, s17
	s_and_b64 s[30:31], s[6:7], exec
	s_cselect_b32 s11, s17, s21
	s_cselect_b32 s37, s16, s20
	s_add_u32 s18, s18, 0x20080
	s_addc_u32 s19, s19, 0
	s_waitcnt lgkmcnt(0)
	s_add_u32 s46, s20, 0x100
	v_mov_b32_e32 v0, 0
	s_addc_u32 s47, s21, 0
	s_mov_b32 s56, -2
	v_mov_b32_e32 v1, v0
	v_mov_b32_e32 v2, v0
	v_mov_b32_e32 v3, v0
	v_mov_b32_e32 v4, v0
	v_mov_b32_e32 v5, v0
	v_mov_b32_e32 v6, v0
	v_mov_b32_e32 v7, v0
	v_mov_b32_e32 v8, v0
	v_mov_b32_e32 v9, v0
	v_mov_b32_e32 v10, v0
	v_mov_b32_e32 v11, v0
	v_mov_b32_e32 v16, v0
	v_mov_b32_e32 v17, v0
	v_mov_b32_e32 v18, v0
	v_mov_b32_e32 v19, v0
	v_mov_b32_e32 v24, v0
	v_mov_b32_e32 v25, v0
	v_mov_b32_e32 v26, v0
	v_mov_b32_e32 v27, v0
	v_mov_b32_e32 v32, v0
	v_mov_b32_e32 v33, v0
	v_mov_b32_e32 v34, v0
	v_mov_b32_e32 v35, v0
	v_mov_b32_e32 v40, v0
	v_mov_b32_e32 v41, v0
	v_mov_b32_e32 v42, v0
	v_mov_b32_e32 v43, v0
	v_mov_b32_e32 v48, v0
	v_mov_b32_e32 v49, v0
	v_mov_b32_e32 v50, v0
	v_mov_b32_e32 v51, v0
	v_mov_b32_e32 v12, v0
	v_mov_b32_e32 v13, v0
	v_mov_b32_e32 v14, v0
	v_mov_b32_e32 v15, v0
	v_mov_b32_e32 v20, v0
	v_mov_b32_e32 v21, v0
	v_mov_b32_e32 v22, v0
	v_mov_b32_e32 v23, v0
	v_mov_b32_e32 v28, v0
	v_mov_b32_e32 v29, v0
	v_mov_b32_e32 v30, v0
	v_mov_b32_e32 v31, v0
	v_mov_b32_e32 v36, v0
	v_mov_b32_e32 v37, v0
	v_mov_b32_e32 v38, v0
	v_mov_b32_e32 v39, v0
	v_mov_b32_e32 v44, v0
	v_mov_b32_e32 v45, v0
	v_mov_b32_e32 v46, v0
	v_mov_b32_e32 v47, v0
	v_mov_b32_e32 v52, v0
	v_mov_b32_e32 v53, v0
	v_mov_b32_e32 v54, v0
	v_mov_b32_e32 v55, v0
	v_mov_b32_e32 v56, v0
	v_mov_b32_e32 v57, v0
	v_mov_b32_e32 v58, v0
	v_mov_b32_e32 v59, v0
	v_mov_b32_e32 v60, v0
	v_mov_b32_e32 v61, v0
	v_mov_b32_e32 v62, v0
	v_mov_b32_e32 v63, v0
	v_mov_b32_e32 v64, v0
	v_mov_b32_e32 v65, v0
	v_mov_b32_e32 v66, v0
	v_mov_b32_e32 v67, v0
	v_mov_b32_e32 v68, v0
	v_mov_b32_e32 v69, v0
	v_mov_b32_e32 v70, v0
	v_mov_b32_e32 v71, v0
	v_mov_b32_e32 v72, v0
	v_mov_b32_e32 v73, v0
	v_mov_b32_e32 v74, v0
	v_mov_b32_e32 v75, v0
	v_mov_b32_e32 v76, v0
	v_mov_b32_e32 v77, v0
	v_mov_b32_e32 v78, v0
	v_mov_b32_e32 v79, v0
	v_mov_b32_e32 v88, v0
	v_mov_b32_e32 v89, v0
	v_mov_b32_e32 v90, v0
	v_mov_b32_e32 v91, v0
	v_mov_b32_e32 v92, v0
	v_mov_b32_e32 v93, v0
	v_mov_b32_e32 v94, v0
	v_mov_b32_e32 v95, v0
	v_mov_b32_e32 v104, v0
	v_mov_b32_e32 v105, v0
	v_mov_b32_e32 v106, v0
	v_mov_b32_e32 v107, v0
	v_mov_b32_e32 v108, v0
	v_mov_b32_e32 v109, v0
	v_mov_b32_e32 v110, v0
	v_mov_b32_e32 v111, v0
	v_mov_b32_e32 v80, v0
	v_mov_b32_e32 v81, v0
	v_mov_b32_e32 v82, v0
	v_mov_b32_e32 v83, v0
	v_mov_b32_e32 v84, v0
	v_mov_b32_e32 v85, v0
	v_mov_b32_e32 v86, v0
	v_mov_b32_e32 v87, v0
	v_mov_b32_e32 v96, v0
	v_mov_b32_e32 v97, v0
	v_mov_b32_e32 v98, v0
	v_mov_b32_e32 v99, v0
	v_mov_b32_e32 v100, v0
	v_mov_b32_e32 v101, v0
	v_mov_b32_e32 v102, v0
	v_mov_b32_e32 v103, v0
	v_mov_b32_e32 v112, v0
	v_mov_b32_e32 v113, v0
	v_mov_b32_e32 v114, v0
	v_mov_b32_e32 v115, v0
	v_mov_b32_e32 v116, v0
	v_mov_b32_e32 v117, v0
	v_mov_b32_e32 v118, v0
	v_mov_b32_e32 v119, v0
	v_mov_b32_e32 v120, v0
	v_mov_b32_e32 v121, v0
	v_mov_b32_e32 v122, v0
	v_mov_b32_e32 v123, v0
	v_mov_b32_e32 v124, v0
	v_mov_b32_e32 v125, v0
	v_mov_b32_e32 v126, v0
	v_mov_b32_e32 v127, v0
	.p2alignl 6, 3212836864

.LBB0_855:
	s_lshl_b64 s[16:17], s[12:13], 18
	s_add_u32 s16, s34, s16
	s_addc_u32 s17, s35, s17
	s_and_b64 s[30:31], s[6:7], exec
	s_cselect_b32 s13, s17, s21
	s_cselect_b32 s15, s16, s20
	s_add_u32 s18, s18, 0x200080
	s_addc_u32 s19, s19, 0
	s_add_u32 s70, s20, 0x100
	v_mov_b32_e32 v0, 0
	s_addc_u32 s71, s21, 0
	s_mov_b32 s72, -2
	v_mov_b32_e32 v1, v0
	v_mov_b32_e32 v2, v0
	v_mov_b32_e32 v3, v0
	v_mov_b32_e32 v4, v0
	v_mov_b32_e32 v5, v0
	v_mov_b32_e32 v6, v0
	v_mov_b32_e32 v7, v0
	v_mov_b32_e32 v8, v0
	v_mov_b32_e32 v9, v0
	v_mov_b32_e32 v10, v0
	v_mov_b32_e32 v11, v0
	v_mov_b32_e32 v16, v0
	v_mov_b32_e32 v17, v0
	v_mov_b32_e32 v18, v0
	v_mov_b32_e32 v19, v0
	v_mov_b32_e32 v24, v0
	v_mov_b32_e32 v25, v0
	v_mov_b32_e32 v26, v0
	v_mov_b32_e32 v27, v0
	v_mov_b32_e32 v32, v0
	v_mov_b32_e32 v33, v0
	v_mov_b32_e32 v34, v0
	v_mov_b32_e32 v35, v0
	v_mov_b32_e32 v40, v0
	v_mov_b32_e32 v41, v0
	v_mov_b32_e32 v42, v0
	v_mov_b32_e32 v43, v0
	v_mov_b32_e32 v48, v0
	v_mov_b32_e32 v49, v0
	v_mov_b32_e32 v50, v0
	v_mov_b32_e32 v51, v0
	v_mov_b32_e32 v12, v0
	v_mov_b32_e32 v13, v0
	v_mov_b32_e32 v14, v0
	v_mov_b32_e32 v15, v0
	v_mov_b32_e32 v20, v0
	v_mov_b32_e32 v21, v0
	v_mov_b32_e32 v22, v0
	v_mov_b32_e32 v23, v0
	v_mov_b32_e32 v28, v0
	v_mov_b32_e32 v29, v0
	v_mov_b32_e32 v30, v0
	v_mov_b32_e32 v31, v0
	v_mov_b32_e32 v36, v0
	v_mov_b32_e32 v37, v0
	v_mov_b32_e32 v38, v0
	v_mov_b32_e32 v39, v0
	v_mov_b32_e32 v44, v0
	v_mov_b32_e32 v45, v0
	v_mov_b32_e32 v46, v0
	v_mov_b32_e32 v47, v0
	v_mov_b32_e32 v52, v0
	v_mov_b32_e32 v53, v0
	v_mov_b32_e32 v54, v0
	v_mov_b32_e32 v55, v0
	v_mov_b32_e32 v56, v0
	v_mov_b32_e32 v57, v0
	v_mov_b32_e32 v58, v0
	v_mov_b32_e32 v59, v0
	v_mov_b32_e32 v60, v0
	v_mov_b32_e32 v61, v0
	v_mov_b32_e32 v62, v0
	v_mov_b32_e32 v63, v0
	v_mov_b32_e32 v64, v0
	v_mov_b32_e32 v65, v0
	v_mov_b32_e32 v66, v0
	v_mov_b32_e32 v67, v0
	v_mov_b32_e32 v68, v0
	v_mov_b32_e32 v69, v0
	v_mov_b32_e32 v70, v0
	v_mov_b32_e32 v71, v0
	v_mov_b32_e32 v72, v0
	v_mov_b32_e32 v73, v0
	v_mov_b32_e32 v74, v0
	v_mov_b32_e32 v75, v0
	v_mov_b32_e32 v80, v0
	v_mov_b32_e32 v81, v0
	v_mov_b32_e32 v82, v0
	v_mov_b32_e32 v83, v0
	v_mov_b32_e32 v88, v0
	v_mov_b32_e32 v89, v0
	v_mov_b32_e32 v90, v0
	v_mov_b32_e32 v91, v0
	v_mov_b32_e32 v92, v0
	v_mov_b32_e32 v93, v0
	v_mov_b32_e32 v94, v0
	v_mov_b32_e32 v95, v0
	v_mov_b32_e32 v104, v0
	v_mov_b32_e32 v105, v0
	v_mov_b32_e32 v106, v0
	v_mov_b32_e32 v107, v0
	v_mov_b32_e32 v108, v0
	v_mov_b32_e32 v109, v0
	v_mov_b32_e32 v110, v0
	v_mov_b32_e32 v111, v0
	v_mov_b32_e32 v76, v0
	v_mov_b32_e32 v77, v0
	v_mov_b32_e32 v78, v0
	v_mov_b32_e32 v79, v0
	v_mov_b32_e32 v84, v0
	v_mov_b32_e32 v85, v0
	v_mov_b32_e32 v86, v0
	v_mov_b32_e32 v87, v0
	v_mov_b32_e32 v96, v0
	v_mov_b32_e32 v97, v0
	v_mov_b32_e32 v98, v0
	v_mov_b32_e32 v99, v0
	v_mov_b32_e32 v100, v0
	v_mov_b32_e32 v101, v0
	v_mov_b32_e32 v102, v0
	v_mov_b32_e32 v103, v0
	v_mov_b32_e32 v112, v0
	v_mov_b32_e32 v113, v0
	v_mov_b32_e32 v114, v0
	v_mov_b32_e32 v115, v0
	v_mov_b32_e32 v116, v0
	v_mov_b32_e32 v117, v0
	v_mov_b32_e32 v118, v0
	v_mov_b32_e32 v119, v0
	v_mov_b32_e32 v120, v0
	v_mov_b32_e32 v121, v0
	v_mov_b32_e32 v122, v0
	v_mov_b32_e32 v123, v0
	v_mov_b32_e32 v124, v0
	v_mov_b32_e32 v125, v0
	v_mov_b32_e32 v126, v0
	v_mov_b32_e32 v127, v0
	.p2alignl 6, 3212836864

.LBB0_906:
	s_ashr_i32 s13, s12, 31
	s_lshl_b64 s[14:15], s[12:13], 21
	s_add_u32 s14, s52, s14
	s_addc_u32 s15, s53, s15
	s_and_b64 s[16:17], s[6:7], exec
	s_cselect_b32 s13, s15, s19
	s_cselect_b32 s69, s14, s18
	s_ashr_i32 s11, s10, 31
	s_lshl_b64 s[16:17], s[10:11], 21
	s_add_u32 s16, s34, s16
	s_addc_u32 s17, s35, s17
	s_and_b64 s[30:31], s[6:7], exec
	s_cselect_b32 s11, s17, s21
	s_cselect_b32 s70, s16, s20
	s_add_u32 s18, s18, 0x100080
	s_addc_u32 s19, s19, 0
	s_add_u32 s71, s20, 0x100
	v_mov_b32_e32 v0, 0
	s_addc_u32 s72, s21, 0
	s_mov_b32 s73, -2
	v_mov_b32_e32 v1, v0
	v_mov_b32_e32 v2, v0
	v_mov_b32_e32 v3, v0
	v_mov_b32_e32 v4, v0
	v_mov_b32_e32 v5, v0
	v_mov_b32_e32 v6, v0
	v_mov_b32_e32 v7, v0
	v_mov_b32_e32 v8, v0
	v_mov_b32_e32 v9, v0
	v_mov_b32_e32 v10, v0
	v_mov_b32_e32 v11, v0
	v_mov_b32_e32 v16, v0
	v_mov_b32_e32 v17, v0
	v_mov_b32_e32 v18, v0
	v_mov_b32_e32 v19, v0
	v_mov_b32_e32 v24, v0
	v_mov_b32_e32 v25, v0
	v_mov_b32_e32 v26, v0
	v_mov_b32_e32 v27, v0
	v_mov_b32_e32 v32, v0
	v_mov_b32_e32 v33, v0
	v_mov_b32_e32 v34, v0
	v_mov_b32_e32 v35, v0
	v_mov_b32_e32 v40, v0
	v_mov_b32_e32 v41, v0
	v_mov_b32_e32 v42, v0
	v_mov_b32_e32 v43, v0
	v_mov_b32_e32 v48, v0
	v_mov_b32_e32 v49, v0
	v_mov_b32_e32 v50, v0
	v_mov_b32_e32 v51, v0
	v_mov_b32_e32 v12, v0
	v_mov_b32_e32 v13, v0
	v_mov_b32_e32 v14, v0
	v_mov_b32_e32 v15, v0
	v_mov_b32_e32 v20, v0
	v_mov_b32_e32 v21, v0
	v_mov_b32_e32 v22, v0
	v_mov_b32_e32 v23, v0
	v_mov_b32_e32 v28, v0
	v_mov_b32_e32 v29, v0
	v_mov_b32_e32 v30, v0
	v_mov_b32_e32 v31, v0
	v_mov_b32_e32 v36, v0
	v_mov_b32_e32 v37, v0
	v_mov_b32_e32 v38, v0
	v_mov_b32_e32 v39, v0
	v_mov_b32_e32 v44, v0
	v_mov_b32_e32 v45, v0
	v_mov_b32_e32 v46, v0
	v_mov_b32_e32 v47, v0
	v_mov_b32_e32 v52, v0
	v_mov_b32_e32 v53, v0
	v_mov_b32_e32 v54, v0
	v_mov_b32_e32 v55, v0
	v_mov_b32_e32 v56, v0
	v_mov_b32_e32 v57, v0
	v_mov_b32_e32 v58, v0
	v_mov_b32_e32 v59, v0
	v_mov_b32_e32 v60, v0
	v_mov_b32_e32 v61, v0
	v_mov_b32_e32 v62, v0
	v_mov_b32_e32 v63, v0
	v_mov_b32_e32 v64, v0
	v_mov_b32_e32 v65, v0
	v_mov_b32_e32 v66, v0
	v_mov_b32_e32 v67, v0
	v_mov_b32_e32 v68, v0
	v_mov_b32_e32 v69, v0
	v_mov_b32_e32 v70, v0
	v_mov_b32_e32 v71, v0
	v_mov_b32_e32 v72, v0
	v_mov_b32_e32 v73, v0
	v_mov_b32_e32 v74, v0
	v_mov_b32_e32 v75, v0
	v_mov_b32_e32 v80, v0
	v_mov_b32_e32 v81, v0
	v_mov_b32_e32 v82, v0
	v_mov_b32_e32 v83, v0
	v_mov_b32_e32 v88, v0
	v_mov_b32_e32 v89, v0
	v_mov_b32_e32 v90, v0
	v_mov_b32_e32 v91, v0
	v_mov_b32_e32 v92, v0
	v_mov_b32_e32 v93, v0
	v_mov_b32_e32 v94, v0
	v_mov_b32_e32 v95, v0
	v_mov_b32_e32 v104, v0
	v_mov_b32_e32 v105, v0
	v_mov_b32_e32 v106, v0
	v_mov_b32_e32 v107, v0
	v_mov_b32_e32 v108, v0
	v_mov_b32_e32 v109, v0
	v_mov_b32_e32 v110, v0
	v_mov_b32_e32 v111, v0
	v_mov_b32_e32 v76, v0
	v_mov_b32_e32 v77, v0
	v_mov_b32_e32 v78, v0
	v_mov_b32_e32 v79, v0
	v_mov_b32_e32 v84, v0
	v_mov_b32_e32 v85, v0
	v_mov_b32_e32 v86, v0
	v_mov_b32_e32 v87, v0
	v_mov_b32_e32 v96, v0
	v_mov_b32_e32 v97, v0
	v_mov_b32_e32 v98, v0
	v_mov_b32_e32 v99, v0
	v_mov_b32_e32 v100, v0
	v_mov_b32_e32 v101, v0
	v_mov_b32_e32 v102, v0
	v_mov_b32_e32 v103, v0
	v_mov_b32_e32 v112, v0
	v_mov_b32_e32 v113, v0
	v_mov_b32_e32 v114, v0
	v_mov_b32_e32 v115, v0
	v_mov_b32_e32 v116, v0
	v_mov_b32_e32 v117, v0
	v_mov_b32_e32 v118, v0
	v_mov_b32_e32 v119, v0
	v_mov_b32_e32 v120, v0
	v_mov_b32_e32 v121, v0
	v_mov_b32_e32 v122, v0
	v_mov_b32_e32 v123, v0
	v_mov_b32_e32 v124, v0
	v_mov_b32_e32 v125, v0
	v_mov_b32_e32 v126, v0
	v_mov_b32_e32 v127, v0
	.p2alignl 6, 3212836864

.LBB0_1039:
	s_ashr_i32 s17, s16, 31
	s_lshl_b64 s[18:19], s[16:17], 20
	s_add_u32 s18, s38, s18
	s_addc_u32 s19, s39, s19
	s_and_b64 s[20:21], s[6:7], exec
	s_cselect_b32 s17, s19, s31
	s_cselect_b32 s76, s18, s30
	s_ashr_i32 s11, s10, 31
	s_lshl_b64 s[20:21], s[10:11], 20
	s_add_u32 s20, s41, s20
	s_addc_u32 s21, s43, s21
	s_and_b64 s[36:37], s[6:7], exec
	s_cselect_b32 s11, s21, s35
	s_cselect_b32 s77, s20, s34
	s_add_u32 s30, s30, 0x80080
	s_addc_u32 s31, s31, 0
	s_add_u32 s84, s34, 0x100
	v_mov_b32_e32 v0, 0
	s_addc_u32 s88, s35, 0
	s_mov_b32 s89, -2
	v_mov_b32_e32 v1, v0
	v_mov_b32_e32 v2, v0
	v_mov_b32_e32 v3, v0
	v_mov_b32_e32 v4, v0
	v_mov_b32_e32 v5, v0
	v_mov_b32_e32 v6, v0
	v_mov_b32_e32 v7, v0
	v_mov_b32_e32 v16, v0
	v_mov_b32_e32 v17, v0
	v_mov_b32_e32 v18, v0
	v_mov_b32_e32 v19, v0
	v_mov_b32_e32 v20, v0
	v_mov_b32_e32 v21, v0
	v_mov_b32_e32 v22, v0
	v_mov_b32_e32 v23, v0
	v_mov_b32_e32 v32, v0
	v_mov_b32_e32 v33, v0
	v_mov_b32_e32 v34, v0
	v_mov_b32_e32 v35, v0
	v_mov_b32_e32 v36, v0
	v_mov_b32_e32 v37, v0
	v_mov_b32_e32 v38, v0
	v_mov_b32_e32 v39, v0
	v_mov_b32_e32 v48, v0
	v_mov_b32_e32 v49, v0
	v_mov_b32_e32 v50, v0
	v_mov_b32_e32 v51, v0
	v_mov_b32_e32 v52, v0
	v_mov_b32_e32 v53, v0
	v_mov_b32_e32 v54, v0
	v_mov_b32_e32 v55, v0
	v_mov_b32_e32 v8, v0
	v_mov_b32_e32 v9, v0
	v_mov_b32_e32 v10, v0
	v_mov_b32_e32 v11, v0
	v_mov_b32_e32 v12, v0
	v_mov_b32_e32 v13, v0
	v_mov_b32_e32 v14, v0
	v_mov_b32_e32 v15, v0
	v_mov_b32_e32 v24, v0
	v_mov_b32_e32 v25, v0
	v_mov_b32_e32 v26, v0
	v_mov_b32_e32 v27, v0
	v_mov_b32_e32 v28, v0
	v_mov_b32_e32 v29, v0
	v_mov_b32_e32 v30, v0
	v_mov_b32_e32 v31, v0
	v_mov_b32_e32 v40, v0
	v_mov_b32_e32 v41, v0
	v_mov_b32_e32 v42, v0
	v_mov_b32_e32 v43, v0
	v_mov_b32_e32 v44, v0
	v_mov_b32_e32 v45, v0
	v_mov_b32_e32 v46, v0
	v_mov_b32_e32 v47, v0
	v_mov_b32_e32 v56, v0
	v_mov_b32_e32 v57, v0
	v_mov_b32_e32 v58, v0
	v_mov_b32_e32 v59, v0
	v_mov_b32_e32 v60, v0
	v_mov_b32_e32 v61, v0
	v_mov_b32_e32 v62, v0
	v_mov_b32_e32 v63, v0
	v_mov_b32_e32 v64, v0
	v_mov_b32_e32 v65, v0
	v_mov_b32_e32 v66, v0
	v_mov_b32_e32 v67, v0
	v_mov_b32_e32 v68, v0
	v_mov_b32_e32 v69, v0
	v_mov_b32_e32 v70, v0
	v_mov_b32_e32 v71, v0
	v_mov_b32_e32 v80, v0
	v_mov_b32_e32 v81, v0
	v_mov_b32_e32 v82, v0
	v_mov_b32_e32 v83, v0
	v_mov_b32_e32 v84, v0
	v_mov_b32_e32 v85, v0
	v_mov_b32_e32 v86, v0
	v_mov_b32_e32 v87, v0
	v_mov_b32_e32 v96, v0
	v_mov_b32_e32 v97, v0
	v_mov_b32_e32 v98, v0
	v_mov_b32_e32 v99, v0
	v_mov_b32_e32 v100, v0
	v_mov_b32_e32 v101, v0
	v_mov_b32_e32 v102, v0
	v_mov_b32_e32 v103, v0
	v_mov_b32_e32 v108, v0
	v_mov_b32_e32 v109, v0
	v_mov_b32_e32 v110, v0
	v_mov_b32_e32 v111, v0
	v_mov_b32_e32 v116, v0
	v_mov_b32_e32 v117, v0
	v_mov_b32_e32 v118, v0
	v_mov_b32_e32 v119, v0
	v_mov_b32_e32 v72, v0
	v_mov_b32_e32 v73, v0
	v_mov_b32_e32 v74, v0
	v_mov_b32_e32 v75, v0
	v_mov_b32_e32 v76, v0
	v_mov_b32_e32 v77, v0
	v_mov_b32_e32 v78, v0
	v_mov_b32_e32 v79, v0
	v_mov_b32_e32 v88, v0
	v_mov_b32_e32 v89, v0
	v_mov_b32_e32 v90, v0
	v_mov_b32_e32 v91, v0
	v_mov_b32_e32 v92, v0
	v_mov_b32_e32 v93, v0
	v_mov_b32_e32 v94, v0
	v_mov_b32_e32 v95, v0
	v_mov_b32_e32 v104, v0
	v_mov_b32_e32 v105, v0
	v_mov_b32_e32 v106, v0
	v_mov_b32_e32 v107, v0
	v_mov_b32_e32 v112, v0
	v_mov_b32_e32 v113, v0
	v_mov_b32_e32 v114, v0
	v_mov_b32_e32 v115, v0
	v_mov_b32_e32 v120, v0
	v_mov_b32_e32 v121, v0
	v_mov_b32_e32 v122, v0
	v_mov_b32_e32 v123, v0
	v_mov_b32_e32 v124, v0
	v_mov_b32_e32 v125, v0
	v_mov_b32_e32 v126, v0
	v_mov_b32_e32 v127, v0
	.p2alignl 6, 3212836864

.LBB0_1090:
	s_ashr_i32 s17, s16, 31
	s_lshl_b64 s[18:19], s[16:17], 22
	s_add_u32 s18, s50, s18
	s_addc_u32 s19, s51, s19
	s_and_b64 s[20:21], s[6:7], exec
	s_cselect_b32 s17, s19, s31
	s_cselect_b32 s73, s18, s30
	s_ashr_i32 s11, s10, 31
	s_lshl_b64 s[20:21], s[10:11], 22
	s_add_u32 s20, s41, s20
	s_addc_u32 s21, s43, s21
	s_and_b64 s[36:37], s[6:7], exec
	s_cselect_b32 s11, s21, s35
	s_cselect_b32 s76, s20, s34
	s_add_u32 s30, s30, 0x200080
	s_addc_u32 s31, s31, 0
	s_add_u32 s77, s34, 0x100
	v_mov_b32_e32 v0, 0
	s_addc_u32 s84, s35, 0
	s_mov_b32 s88, -2
	v_mov_b32_e32 v1, v0
	v_mov_b32_e32 v2, v0
	v_mov_b32_e32 v3, v0
	v_mov_b32_e32 v4, v0
	v_mov_b32_e32 v5, v0
	v_mov_b32_e32 v6, v0
	v_mov_b32_e32 v7, v0
	v_mov_b32_e32 v8, v0
	v_mov_b32_e32 v9, v0
	v_mov_b32_e32 v10, v0
	v_mov_b32_e32 v11, v0
	v_mov_b32_e32 v16, v0
	v_mov_b32_e32 v17, v0
	v_mov_b32_e32 v18, v0
	v_mov_b32_e32 v19, v0
	v_mov_b32_e32 v24, v0
	v_mov_b32_e32 v25, v0
	v_mov_b32_e32 v26, v0
	v_mov_b32_e32 v27, v0
	v_mov_b32_e32 v32, v0
	v_mov_b32_e32 v33, v0
	v_mov_b32_e32 v34, v0
	v_mov_b32_e32 v35, v0
	v_mov_b32_e32 v40, v0
	v_mov_b32_e32 v41, v0
	v_mov_b32_e32 v42, v0
	v_mov_b32_e32 v43, v0
	v_mov_b32_e32 v48, v0
	v_mov_b32_e32 v49, v0
	v_mov_b32_e32 v50, v0
	v_mov_b32_e32 v51, v0
	v_mov_b32_e32 v12, v0
	v_mov_b32_e32 v13, v0
	v_mov_b32_e32 v14, v0
	v_mov_b32_e32 v15, v0
	v_mov_b32_e32 v20, v0
	v_mov_b32_e32 v21, v0
	v_mov_b32_e32 v22, v0
	v_mov_b32_e32 v23, v0
	v_mov_b32_e32 v28, v0
	v_mov_b32_e32 v29, v0
	v_mov_b32_e32 v30, v0
	v_mov_b32_e32 v31, v0
	v_mov_b32_e32 v36, v0
	v_mov_b32_e32 v37, v0
	v_mov_b32_e32 v38, v0
	v_mov_b32_e32 v39, v0
	v_mov_b32_e32 v44, v0
	v_mov_b32_e32 v45, v0
	v_mov_b32_e32 v46, v0
	v_mov_b32_e32 v47, v0
	v_mov_b32_e32 v52, v0
	v_mov_b32_e32 v53, v0
	v_mov_b32_e32 v54, v0
	v_mov_b32_e32 v55, v0
	v_mov_b32_e32 v56, v0
	v_mov_b32_e32 v57, v0
	v_mov_b32_e32 v58, v0
	v_mov_b32_e32 v59, v0
	v_mov_b32_e32 v60, v0
	v_mov_b32_e32 v61, v0
	v_mov_b32_e32 v62, v0
	v_mov_b32_e32 v63, v0
	v_mov_b32_e32 v64, v0
	v_mov_b32_e32 v65, v0
	v_mov_b32_e32 v66, v0
	v_mov_b32_e32 v67, v0
	v_mov_b32_e32 v68, v0
	v_mov_b32_e32 v69, v0
	v_mov_b32_e32 v70, v0
	v_mov_b32_e32 v71, v0
	v_mov_b32_e32 v72, v0
	v_mov_b32_e32 v73, v0
	v_mov_b32_e32 v74, v0
	v_mov_b32_e32 v75, v0
	v_mov_b32_e32 v80, v0
	v_mov_b32_e32 v81, v0
	v_mov_b32_e32 v82, v0
	v_mov_b32_e32 v83, v0
	v_mov_b32_e32 v88, v0
	v_mov_b32_e32 v89, v0
	v_mov_b32_e32 v90, v0
	v_mov_b32_e32 v91, v0
	v_mov_b32_e32 v92, v0
	v_mov_b32_e32 v93, v0
	v_mov_b32_e32 v94, v0
	v_mov_b32_e32 v95, v0
	v_mov_b32_e32 v104, v0
	v_mov_b32_e32 v105, v0
	v_mov_b32_e32 v106, v0
	v_mov_b32_e32 v107, v0
	v_mov_b32_e32 v108, v0
	v_mov_b32_e32 v109, v0
	v_mov_b32_e32 v110, v0
	v_mov_b32_e32 v111, v0
	v_mov_b32_e32 v76, v0
	v_mov_b32_e32 v77, v0
	v_mov_b32_e32 v78, v0
	v_mov_b32_e32 v79, v0
	v_mov_b32_e32 v84, v0
	v_mov_b32_e32 v85, v0
	v_mov_b32_e32 v86, v0
	v_mov_b32_e32 v87, v0
	v_mov_b32_e32 v96, v0
	v_mov_b32_e32 v97, v0
	v_mov_b32_e32 v98, v0
	v_mov_b32_e32 v99, v0
	v_mov_b32_e32 v100, v0
	v_mov_b32_e32 v101, v0
	v_mov_b32_e32 v102, v0
	v_mov_b32_e32 v103, v0
	v_mov_b32_e32 v112, v0
	v_mov_b32_e32 v113, v0
	v_mov_b32_e32 v114, v0
	v_mov_b32_e32 v115, v0
	v_mov_b32_e32 v116, v0
	v_mov_b32_e32 v117, v0
	v_mov_b32_e32 v118, v0
	v_mov_b32_e32 v119, v0
	v_mov_b32_e32 v120, v0
	v_mov_b32_e32 v121, v0
	v_mov_b32_e32 v122, v0
	v_mov_b32_e32 v123, v0
	v_mov_b32_e32 v124, v0
	v_mov_b32_e32 v125, v0
	v_mov_b32_e32 v126, v0
	v_mov_b32_e32 v127, v0
	.p2alignl 6, 3212836864
